# layer-0 KV-split: pairs whose partner workgroup also owns a ctx unit hand over 12 tiles instead of 16
# baseline (speedup 1.0000x reference)
.Lkv_upL0:
	s_mov_b32 s28, 0x8940000
	s_movk_i32 s29, 12
	s_cmpk_gt_u32 s19, 0x10f
	s_cbranch_scc1 .LBB0_584
	s_mov_b32 s28, 0x8b80000
	s_movk_i32 s29, 8
	s_branch .LBB0_584

.Lkv_loL0:
	s_movk_i32 s29, 240
	s_cmpk_gt_u32 s19, 0x10f
	s_cbranch_scc1 .LBB0_584
	s_movk_i32 s29, 244
	s_branch .LBB0_584
